# attention tile loops: waves 4-7 staggered behind waves 0-3 by s_sleep 2 (128 cycles) after each tile barrier so the two waves of a SIMD de-overlap their MFMA and VALU phases
# speedup vs baseline: 1.0109x; 1.0013x over previous
.LBB0_1652:
	s_or_b64 exec, exec, s[8:9]
	s_barrier
	v_readfirstlane_b32 s101, v0
	s_bitcmp1_b32 s101, 8
	s_cbranch_scc0 .Lmy_stagger_ma
	s_sleep 2

.LBB0_1707:
	s_or_b64 exec, exec, s[34:35]
	s_barrier
	v_readfirstlane_b32 s101, v0
	s_bitcmp1_b32 s101, 8
	s_cbranch_scc0 .Lmy_stagger_dl
	s_sleep 2
